# Y0 deferred to scan 3 (rows 0-95 by producer waves), single-round epilogue gather of 32 rows
# speedup vs baseline: 1.0364x; 1.0145x over previous
.LBB1_67:
	v_readlane_b32 s44, v14, 0
	v_readlane_b32 s45, v14, 1
	v_readlane_b32 s46, v14, 2
	v_readlane_b32 s47, v14, 3
	v_readlane_b32 s48, v14, 4
	v_readlane_b32 s49, v14, 5
	v_readlane_b32 s50, v14, 6
	v_readlane_b32 s51, v14, 7
	v_readlane_b32 s52, v14, 8
	v_readlane_b32 s53, v14, 9
	v_readlane_b32 s54, v14, 10
	v_readlane_b32 s55, v14, 11
	v_readlane_b32 s56, v14, 12
	v_readlane_b32 s57, v14, 13
	v_readlane_b32 s58, v14, 14
	v_readlane_b32 s59, v14, 15
	v_readlane_b32 s60, v14, 16
	v_readlane_b32 s61, v14, 17
	v_readlane_b32 s62, v14, 18
	v_readlane_b32 s63, v14, 19
	v_readlane_b32 s64, v14, 20
	v_readlane_b32 s65, v14, 21
	v_readlane_b32 s66, v14, 22
	v_readlane_b32 s67, v14, 23
	v_readlane_b32 s68, v14, 24
	v_readlane_b32 s69, v14, 25
	v_readlane_b32 s70, v14, 26
	v_readlane_b32 s71, v14, 27
	v_readlane_b32 s72, v14, 28
	v_readlane_b32 s73, v14, 29
	v_readlane_b32 s74, v14, 30
	v_readlane_b32 s75, v14, 31
	s_mov_b32 s76, 0xfffff400
	s_mov_b32 s77, -1
	v_lshl_add_u64 v[150:151], v[168:169], 0, s[76:77]
	s_mov_b32 s76, 0x1400
	s_mov_b32 s77, 0
	v_lshl_add_u64 v[152:153], v[168:169], 0, s[76:77]
	s_mov_b32 s76, 0x3400
	s_mov_b32 s77, 0
	v_lshl_add_u64 v[154:155], v[168:169], 0, s[76:77]
	s_mov_b32 s76, 0x5400
	s_mov_b32 s77, 0
	v_lshl_add_u64 v[156:157], v[168:169], 0, s[76:77]
	v_lshl_or_b32 v146, s44, 10, v162
	v_lshl_or_b32 v147, s45, 10, v162
	v_lshl_or_b32 v148, s46, 10, v162
	v_lshl_or_b32 v149, s47, 10, v162
	v_lshl_or_b32 v158, s48, 10, v162
	v_lshl_or_b32 v159, s49, 10, v162
	v_lshl_or_b32 v160, s50, 10, v162
	v_lshl_or_b32 v161, s51, 10, v162
	global_load_dwordx4 v[2:5], v146, s[18:19]
	global_load_dwordx4 v[6:9], v147, s[18:19]
	global_load_dwordx4 v[10:13], v148, s[18:19]
	global_load_dwordx4 v[14:17], v149, s[18:19]
	global_load_dwordx4 v[18:21], v158, s[18:19]
	global_load_dwordx4 v[22:25], v159, s[18:19]
	global_load_dwordx4 v[26:29], v160, s[18:19]
	global_load_dwordx4 v[30:33], v161, s[18:19]
	v_lshl_or_b32 v146, s52, 10, v162
	v_lshl_or_b32 v147, s53, 10, v162
	v_lshl_or_b32 v148, s54, 10, v162
	v_lshl_or_b32 v149, s55, 10, v162
	v_lshl_or_b32 v158, s56, 10, v162
	v_lshl_or_b32 v159, s57, 10, v162
	v_lshl_or_b32 v160, s58, 10, v162
	v_lshl_or_b32 v161, s59, 10, v162
	global_load_dwordx4 v[34:37], v146, s[18:19]
	global_load_dwordx4 v[38:41], v147, s[18:19]
	global_load_dwordx4 v[42:45], v148, s[18:19]
	global_load_dwordx4 v[46:49], v149, s[18:19]
	global_load_dwordx4 v[50:53], v158, s[18:19]
	global_load_dwordx4 v[54:57], v159, s[18:19]
	global_load_dwordx4 v[58:61], v160, s[18:19]
	global_load_dwordx4 v[62:65], v161, s[18:19]
	v_lshl_or_b32 v146, s60, 10, v162
	v_lshl_or_b32 v147, s61, 10, v162
	v_lshl_or_b32 v148, s62, 10, v162
	v_lshl_or_b32 v149, s63, 10, v162
	v_lshl_or_b32 v158, s64, 10, v162
	v_lshl_or_b32 v159, s65, 10, v162
	v_lshl_or_b32 v160, s66, 10, v162
	v_lshl_or_b32 v161, s67, 10, v162
	global_load_dwordx4 v[66:69], v146, s[18:19]
	global_load_dwordx4 v[70:73], v147, s[18:19]
	global_load_dwordx4 v[74:77], v148, s[18:19]
	global_load_dwordx4 v[78:81], v149, s[18:19]
	global_load_dwordx4 v[82:85], v158, s[18:19]
	global_load_dwordx4 v[86:89], v159, s[18:19]
	global_load_dwordx4 v[90:93], v160, s[18:19]
	global_load_dwordx4 v[94:97], v161, s[18:19]
	v_lshl_or_b32 v146, s68, 10, v162
	v_lshl_or_b32 v147, s69, 10, v162
	v_lshl_or_b32 v148, s70, 10, v162
	v_lshl_or_b32 v149, s71, 10, v162
	v_lshl_or_b32 v158, s72, 10, v162
	v_lshl_or_b32 v159, s73, 10, v162
	v_lshl_or_b32 v160, s74, 10, v162
	v_lshl_or_b32 v161, s75, 10, v162
	global_load_dwordx4 v[114:117], v146, s[18:19]
	global_load_dwordx4 v[118:121], v147, s[18:19]
	global_load_dwordx4 v[122:125], v148, s[18:19]
	global_load_dwordx4 v[126:129], v149, s[18:19]
	global_load_dwordx4 v[130:133], v158, s[18:19]
	global_load_dwordx4 v[134:137], v159, s[18:19]
	global_load_dwordx4 v[138:141], v160, s[18:19]
	global_load_dwordx4 v[142:145], v161, s[18:19]
	s_waitcnt vmcnt(31)
	global_store_dwordx4 v[150:151], v[2:5], off offset:-4096 nt
	s_waitcnt vmcnt(31)
	global_store_dwordx4 v[150:151], v[6:9], off offset:-3072 nt
	s_waitcnt vmcnt(31)
	global_store_dwordx4 v[150:151], v[10:13], off offset:-2048 nt
	s_waitcnt vmcnt(31)
	global_store_dwordx4 v[150:151], v[14:17], off offset:-1024 nt
	s_waitcnt vmcnt(31)
	global_store_dwordx4 v[150:151], v[18:21], off offset:0 nt
	s_waitcnt vmcnt(31)
	global_store_dwordx4 v[150:151], v[22:25], off offset:1024 nt
	s_waitcnt vmcnt(31)
	global_store_dwordx4 v[150:151], v[26:29], off offset:2048 nt
	s_waitcnt vmcnt(31)
	global_store_dwordx4 v[150:151], v[30:33], off offset:3072 nt
	s_waitcnt vmcnt(31)
	global_store_dwordx4 v[152:153], v[34:37], off offset:-4096 nt
	s_waitcnt vmcnt(31)
	global_store_dwordx4 v[152:153], v[38:41], off offset:-3072 nt
	s_waitcnt vmcnt(31)
	global_store_dwordx4 v[152:153], v[42:45], off offset:-2048 nt
	s_waitcnt vmcnt(31)
	global_store_dwordx4 v[152:153], v[46:49], off offset:-1024 nt
	s_waitcnt vmcnt(31)
	global_store_dwordx4 v[152:153], v[50:53], off offset:0 nt
	s_waitcnt vmcnt(31)
	global_store_dwordx4 v[152:153], v[54:57], off offset:1024 nt
	s_waitcnt vmcnt(31)
	global_store_dwordx4 v[152:153], v[58:61], off offset:2048 nt
	s_waitcnt vmcnt(31)
	global_store_dwordx4 v[152:153], v[62:65], off offset:3072 nt
	s_waitcnt vmcnt(31)
	global_store_dwordx4 v[154:155], v[66:69], off offset:-4096 nt
	s_waitcnt vmcnt(31)
	global_store_dwordx4 v[154:155], v[70:73], off offset:-3072 nt
	s_waitcnt vmcnt(31)
	global_store_dwordx4 v[154:155], v[74:77], off offset:-2048 nt
	s_waitcnt vmcnt(31)
	global_store_dwordx4 v[154:155], v[78:81], off offset:-1024 nt
	s_waitcnt vmcnt(31)
	global_store_dwordx4 v[154:155], v[82:85], off offset:0 nt
	s_waitcnt vmcnt(31)
	global_store_dwordx4 v[154:155], v[86:89], off offset:1024 nt
	s_waitcnt vmcnt(31)
	global_store_dwordx4 v[154:155], v[90:93], off offset:2048 nt
	s_waitcnt vmcnt(31)
	global_store_dwordx4 v[154:155], v[94:97], off offset:3072 nt
	s_waitcnt vmcnt(31)
	global_store_dwordx4 v[156:157], v[114:117], off offset:-4096 nt
	s_waitcnt vmcnt(31)
	global_store_dwordx4 v[156:157], v[118:121], off offset:-3072 nt
	s_waitcnt vmcnt(31)
	global_store_dwordx4 v[156:157], v[122:125], off offset:-2048 nt
	s_waitcnt vmcnt(31)
	global_store_dwordx4 v[156:157], v[126:129], off offset:-1024 nt
	s_waitcnt vmcnt(31)
	global_store_dwordx4 v[156:157], v[130:133], off offset:0 nt
	s_waitcnt vmcnt(31)
	global_store_dwordx4 v[156:157], v[134:137], off offset:1024 nt
	s_waitcnt vmcnt(31)
	global_store_dwordx4 v[156:157], v[138:141], off offset:2048 nt
	s_waitcnt vmcnt(31)
	global_store_dwordx4 v[156:157], v[142:145], off offset:3072 nt
	s_branch .LBB1_5

.LBB1_151:
	s_barrier
	s_add_i32 s100, s98, 0xfffe7f90
	s_add_i32 s6, s33, -5
	s_lshl_b32 s6, s6, 3
	s_add_i32 s100, s100, s6
	s_lshl_b32 s7, s6, 2
	s_add_i32 s7, s7, 0x22640
	v_mov_b32_e32 v114, s7
	ds_read_b128 v[2:5], v114 offset:0
	ds_read_b128 v[6:9], v114 offset:16
	s_waitcnt lgkmcnt(0)
	v_lshl_or_b32 v106, v2, 10, v162
	v_lshl_or_b32 v107, v3, 10, v162
	v_lshl_or_b32 v108, v4, 10, v162
	v_lshl_or_b32 v109, v5, 10, v162
	v_lshl_or_b32 v110, v6, 10, v162
	v_lshl_or_b32 v111, v7, 10, v162
	v_lshl_or_b32 v112, v8, 10, v162
	v_lshl_or_b32 v113, v9, 10, v162
	global_load_dwordx4 v[10:13], v106, s[18:19]
	global_load_dwordx4 v[14:17], v107, s[18:19]
	global_load_dwordx4 v[18:21], v108, s[18:19]
	global_load_dwordx4 v[22:25], v109, s[18:19]
	global_load_dwordx4 v[26:29], v110, s[18:19]
	global_load_dwordx4 v[30:33], v111, s[18:19]
	global_load_dwordx4 v[34:37], v112, s[18:19]
	global_load_dwordx4 v[38:41], v113, s[18:19]
	ds_read_b128 v[2:5], v114 offset:64
	ds_read_b128 v[6:9], v114 offset:80
	s_waitcnt lgkmcnt(0)
	v_lshl_or_b32 v106, v2, 10, v162
	v_lshl_or_b32 v107, v3, 10, v162
	v_lshl_or_b32 v108, v4, 10, v162
	v_lshl_or_b32 v109, v5, 10, v162
	v_lshl_or_b32 v110, v6, 10, v162
	v_lshl_or_b32 v111, v7, 10, v162
	v_lshl_or_b32 v112, v8, 10, v162
	v_lshl_or_b32 v113, v9, 10, v162
	global_load_dwordx4 v[42:45], v106, s[18:19]
	global_load_dwordx4 v[46:49], v107, s[18:19]
	global_load_dwordx4 v[50:53], v108, s[18:19]
	global_load_dwordx4 v[54:57], v109, s[18:19]
	global_load_dwordx4 v[58:61], v110, s[18:19]
	global_load_dwordx4 v[62:65], v111, s[18:19]
	global_load_dwordx4 v[66:69], v112, s[18:19]
	global_load_dwordx4 v[70:73], v113, s[18:19]
	ds_read_b128 v[2:5], v114 offset:128
	ds_read_b128 v[6:9], v114 offset:144
	s_waitcnt lgkmcnt(0)
	v_lshl_or_b32 v106, v2, 10, v162
	v_lshl_or_b32 v107, v3, 10, v162
	v_lshl_or_b32 v108, v4, 10, v162
	v_lshl_or_b32 v109, v5, 10, v162
	v_lshl_or_b32 v110, v6, 10, v162
	v_lshl_or_b32 v111, v7, 10, v162
	v_lshl_or_b32 v112, v8, 10, v162
	v_lshl_or_b32 v113, v9, 10, v162
	global_load_dwordx4 v[74:77], v106, s[18:19]
	global_load_dwordx4 v[78:81], v107, s[18:19]
	global_load_dwordx4 v[82:85], v108, s[18:19]
	global_load_dwordx4 v[86:89], v109, s[18:19]
	global_load_dwordx4 v[90:93], v110, s[18:19]
	global_load_dwordx4 v[94:97], v111, s[18:19]
	global_load_dwordx4 v[98:101], v112, s[18:19]
	global_load_dwordx4 v[102:105], v113, s[18:19]
	s_add_i32 s2, s100, 0
	s_lshl_b32 s2, s2, 10
	s_add_u32 s2, s14, s2
	s_addc_u32 s3, s15, 0
	s_add_u32 s4, s2, 0x1000
	s_addc_u32 s5, s3, 0
	s_waitcnt vmcnt(16)
	global_store_dwordx4 v162, v[10:13], s[2:3] offset:0 nt
	global_store_dwordx4 v162, v[14:17], s[2:3] offset:1024 nt
	global_store_dwordx4 v162, v[18:21], s[2:3] offset:2048 nt
	global_store_dwordx4 v162, v[22:25], s[2:3] offset:3072 nt
	global_store_dwordx4 v162, v[26:29], s[4:5] offset:0 nt
	global_store_dwordx4 v162, v[30:33], s[4:5] offset:1024 nt
	global_store_dwordx4 v162, v[34:37], s[4:5] offset:2048 nt
	global_store_dwordx4 v162, v[38:41], s[4:5] offset:3072 nt
	s_barrier
	ds_read_b128 v[2:5], v114 offset:192
	ds_read_b128 v[6:9], v114 offset:208
	s_waitcnt lgkmcnt(0)
	v_lshl_or_b32 v106, v2, 10, v162
	v_lshl_or_b32 v107, v3, 10, v162
	v_lshl_or_b32 v108, v4, 10, v162
	v_lshl_or_b32 v109, v5, 10, v162
	v_lshl_or_b32 v110, v6, 10, v162
	v_lshl_or_b32 v111, v7, 10, v162
	v_lshl_or_b32 v112, v8, 10, v162
	v_lshl_or_b32 v113, v9, 10, v162
	global_load_dwordx4 v[10:13], v106, s[18:19]
	global_load_dwordx4 v[14:17], v107, s[18:19]
	global_load_dwordx4 v[18:21], v108, s[18:19]
	global_load_dwordx4 v[22:25], v109, s[18:19]
	global_load_dwordx4 v[26:29], v110, s[18:19]
	global_load_dwordx4 v[30:33], v111, s[18:19]
	global_load_dwordx4 v[34:37], v112, s[18:19]
	global_load_dwordx4 v[38:41], v113, s[18:19]
	s_add_i32 s2, s100, 16
	s_lshl_b32 s2, s2, 10
	s_add_u32 s2, s14, s2
	s_addc_u32 s3, s15, 0
	s_add_u32 s4, s2, 0x1000
	s_addc_u32 s5, s3, 0
	s_waitcnt vmcnt(24)
	global_store_dwordx4 v162, v[42:45], s[2:3] offset:0 nt
	global_store_dwordx4 v162, v[46:49], s[2:3] offset:1024 nt
	global_store_dwordx4 v162, v[50:53], s[2:3] offset:2048 nt
	global_store_dwordx4 v162, v[54:57], s[2:3] offset:3072 nt
	global_store_dwordx4 v162, v[58:61], s[4:5] offset:0 nt
	global_store_dwordx4 v162, v[62:65], s[4:5] offset:1024 nt
	global_store_dwordx4 v162, v[66:69], s[4:5] offset:2048 nt
	global_store_dwordx4 v162, v[70:73], s[4:5] offset:3072 nt
	s_barrier
	ds_read_b128 v[2:5], v114 offset:256
	ds_read_b128 v[6:9], v114 offset:272
	s_waitcnt lgkmcnt(0)
	v_lshl_or_b32 v106, v2, 10, v162
	v_lshl_or_b32 v107, v3, 10, v162
	v_lshl_or_b32 v108, v4, 10, v162
	v_lshl_or_b32 v109, v5, 10, v162
	v_lshl_or_b32 v110, v6, 10, v162
	v_lshl_or_b32 v111, v7, 10, v162
	v_lshl_or_b32 v112, v8, 10, v162
	v_lshl_or_b32 v113, v9, 10, v162
	global_load_dwordx4 v[42:45], v106, s[18:19]
	global_load_dwordx4 v[46:49], v107, s[18:19]
	global_load_dwordx4 v[50:53], v108, s[18:19]
	global_load_dwordx4 v[54:57], v109, s[18:19]
	global_load_dwordx4 v[58:61], v110, s[18:19]
	global_load_dwordx4 v[62:65], v111, s[18:19]
	global_load_dwordx4 v[66:69], v112, s[18:19]
	global_load_dwordx4 v[70:73], v113, s[18:19]
	s_add_i32 s2, s100, 32
	s_lshl_b32 s2, s2, 10
	s_add_u32 s2, s14, s2
	s_addc_u32 s3, s15, 0
	s_add_u32 s4, s2, 0x1000
	s_addc_u32 s5, s3, 0
	s_waitcnt vmcnt(32)
	global_store_dwordx4 v162, v[74:77], s[2:3] offset:0 nt
	global_store_dwordx4 v162, v[78:81], s[2:3] offset:1024 nt
	global_store_dwordx4 v162, v[82:85], s[2:3] offset:2048 nt
	global_store_dwordx4 v162, v[86:89], s[2:3] offset:3072 nt
	global_store_dwordx4 v162, v[90:93], s[4:5] offset:0 nt
	global_store_dwordx4 v162, v[94:97], s[4:5] offset:1024 nt
	global_store_dwordx4 v162, v[98:101], s[4:5] offset:2048 nt
	global_store_dwordx4 v162, v[102:105], s[4:5] offset:3072 nt
	s_barrier
	ds_read_b128 v[2:5], v114 offset:320
	ds_read_b128 v[6:9], v114 offset:336
	s_waitcnt lgkmcnt(0)
	v_lshl_or_b32 v106, v2, 10, v162
	v_lshl_or_b32 v107, v3, 10, v162
	v_lshl_or_b32 v108, v4, 10, v162
	v_lshl_or_b32 v109, v5, 10, v162
	v_lshl_or_b32 v110, v6, 10, v162
	v_lshl_or_b32 v111, v7, 10, v162
	v_lshl_or_b32 v112, v8, 10, v162
	v_lshl_or_b32 v113, v9, 10, v162
	global_load_dwordx4 v[74:77], v106, s[18:19]
	global_load_dwordx4 v[78:81], v107, s[18:19]
	global_load_dwordx4 v[82:85], v108, s[18:19]
	global_load_dwordx4 v[86:89], v109, s[18:19]
	global_load_dwordx4 v[90:93], v110, s[18:19]
	global_load_dwordx4 v[94:97], v111, s[18:19]
	global_load_dwordx4 v[98:101], v112, s[18:19]
	global_load_dwordx4 v[102:105], v113, s[18:19]
	s_add_i32 s2, s100, 48
	s_lshl_b32 s2, s2, 10
	s_add_u32 s2, s14, s2
	s_addc_u32 s3, s15, 0
	s_add_u32 s4, s2, 0x1000
	s_addc_u32 s5, s3, 0
	s_waitcnt vmcnt(32)
	global_store_dwordx4 v162, v[10:13], s[2:3] offset:0 nt
	global_store_dwordx4 v162, v[14:17], s[2:3] offset:1024 nt
	global_store_dwordx4 v162, v[18:21], s[2:3] offset:2048 nt
	global_store_dwordx4 v162, v[22:25], s[2:3] offset:3072 nt
	global_store_dwordx4 v162, v[26:29], s[4:5] offset:0 nt
	global_store_dwordx4 v162, v[30:33], s[4:5] offset:1024 nt
	global_store_dwordx4 v162, v[34:37], s[4:5] offset:2048 nt
	global_store_dwordx4 v162, v[38:41], s[4:5] offset:3072 nt
	s_barrier
	s_add_i32 s2, s100, 64
	s_lshl_b32 s2, s2, 10
	s_add_u32 s2, s14, s2
	s_addc_u32 s3, s15, 0
	s_add_u32 s4, s2, 0x1000
	s_addc_u32 s5, s3, 0
	s_waitcnt vmcnt(24)
	global_store_dwordx4 v162, v[42:45], s[2:3] offset:0 nt
	global_store_dwordx4 v162, v[46:49], s[2:3] offset:1024 nt
	global_store_dwordx4 v162, v[50:53], s[2:3] offset:2048 nt
	global_store_dwordx4 v162, v[54:57], s[2:3] offset:3072 nt
	global_store_dwordx4 v162, v[58:61], s[4:5] offset:0 nt
	global_store_dwordx4 v162, v[62:65], s[4:5] offset:1024 nt
	global_store_dwordx4 v162, v[66:69], s[4:5] offset:2048 nt
	global_store_dwordx4 v162, v[70:73], s[4:5] offset:3072 nt
	s_barrier
	s_add_i32 s2, s100, 80
	s_lshl_b32 s2, s2, 10
	s_add_u32 s2, s14, s2
	s_addc_u32 s3, s15, 0
	s_add_u32 s4, s2, 0x1000
	s_addc_u32 s5, s3, 0
	s_waitcnt vmcnt(16)
	global_store_dwordx4 v162, v[74:77], s[2:3] offset:0 nt
	global_store_dwordx4 v162, v[78:81], s[2:3] offset:1024 nt
	global_store_dwordx4 v162, v[82:85], s[2:3] offset:2048 nt
	global_store_dwordx4 v162, v[86:89], s[2:3] offset:3072 nt
	global_store_dwordx4 v162, v[90:93], s[4:5] offset:0 nt
	global_store_dwordx4 v162, v[94:97], s[4:5] offset:1024 nt
	global_store_dwordx4 v162, v[98:101], s[4:5] offset:2048 nt
	global_store_dwordx4 v162, v[102:105], s[4:5] offset:3072 nt
	s_barrier
	s_barrier
	s_barrier
	s_barrier
	ds_read_b32 v1, v1
	s_waitcnt lgkmcnt(0)
	v_cmp_gt_i32_e32 vcc, 1, v1
	s_cbranch_vccnz .LBB1_154
